# nt hint extended: expert-output gathers in the layer-1 and final rowpasses, and the final output stores
# speedup vs baseline: 1.0028x; 1.0007x over previous
.LBB0_141:
	s_add_i32 s7, s14, 2
	s_cmp_ge_i32 s14, s12
	s_cselect_b64 s[38:39], -1, 0
	s_cmp_lt_i32 s14, s12
	s_waitcnt vmcnt(0)
	v_mov_b32_e32 v112, v32
	s_cselect_b32 s26, s7, s14
	v_lshlrev_b64 v[36:37], 10, v[112:113]
	v_mov_b32_e32 v112, v33
	s_ashr_i32 s27, s26, 31
	v_lshlrev_b64 v[32:33], 10, v[112:113]
	v_mov_b32_e32 v112, v34
	s_lshl_b64 s[26:27], s[26:27], 4
	v_readlane_b32 s28, v252, 8
	v_lshl_add_u64 v[72:73], s[94:95], 0, v[68:69]
	s_mov_b32 s15, 0xed40000
	v_lshlrev_b64 v[38:39], 10, v[112:113]
	v_mov_b32_e32 v112, v35
	v_readlane_b32 s29, v252, 9
	s_add_u32 s26, s28, s26
	v_add_co_u32_e32 v86, vcc, s15, v72
	v_lshlrev_b64 v[34:35], 10, v[112:113]
	s_addc_u32 s27, s29, s27
	v_addc_co_u32_e32 v87, vcc, 0, v73, vcc
	v_lshl_add_u64 v[36:37], v[62:63], 0, v[36:37]
	v_lshl_add_u64 v[32:33], v[62:63], 0, v[32:33]
	v_lshl_add_u64 v[38:39], v[62:63], 0, v[38:39]
	v_lshl_add_u64 v[34:35], v[62:63], 0, v[34:35]
	v_mov_b32_e32 v112, v56
	global_load_dwordx4 v[8:11], v113, s[26:27] offset:16
	global_load_dwordx4 v[12:15], v113, s[26:27]
	global_load_dwordx4 v[52:55], v[86:87], off
	global_load_dwordx4 v[48:51], v[86:87], off offset:1024
	global_load_dwordx2 v[118:119], v[36:37], off nt
	global_load_dwordx2 v[116:117], v[32:33], off nt
	global_load_dwordx2 v[106:107], v[32:33], off offset:512 nt
	global_load_dwordx2 v[108:109], v[36:37], off offset:512 nt
	global_load_dwordx2 v[114:115], v[38:39], off nt
	global_load_dwordx2 v[110:111], v[34:35], off nt
	global_load_dwordx2 v[102:103], v[34:35], off offset:512 nt
	global_load_dwordx2 v[104:105], v[38:39], off offset:512 nt
	s_nop 0
	global_load_dwordx4 v[36:39], v[86:87], off offset:2048
	global_load_dwordx4 v[32:35], v[86:87], off offset:3072
	v_lshlrev_b64 v[86:87], 10, v[112:113]
	v_mov_b32_e32 v112, v57
	v_lshlrev_b64 v[56:57], 10, v[112:113]
	v_mov_b32_e32 v112, v58
	v_lshl_add_u64 v[92:93], v[62:63], 0, v[86:87]
	v_lshlrev_b64 v[86:87], 10, v[112:113]
	v_mov_b32_e32 v112, v59
	v_lshlrev_b64 v[58:59], 10, v[112:113]
	v_lshl_add_u64 v[56:57], v[62:63], 0, v[56:57]
	v_lshl_add_u64 v[58:59], v[62:63], 0, v[58:59]
	v_lshl_add_u64 v[120:121], v[62:63], 0, v[86:87]
	global_load_dwordx2 v[100:101], v[92:93], off nt
	global_load_dwordx2 v[98:99], v[56:57], off nt
	global_load_dwordx2 v[86:87], v[56:57], off offset:512 nt
	s_nop 0
	global_load_dwordx2 v[92:93], v[92:93], off offset:512 nt
	s_nop 0
	global_load_dwordx2 v[96:97], v[120:121], off nt
	global_load_dwordx2 v[94:95], v[58:59], off nt
	global_load_dwordx2 v[56:57], v[58:59], off offset:512 nt
	s_nop 0
	global_load_dwordx2 v[58:59], v[120:121], off offset:512 nt
	s_mul_hi_i32 s15, s14, 0x78787879
	s_lshr_b32 s25, s15, 31
	s_ashr_i32 s15, s15, 11
	s_add_i32 s15, s15, s25
	s_mul_i32 s25, s15, 0xffffef00
	s_add_i32 s25, s14, s25
	s_cmpk_gt_i32 s25, 0xff
	s_cselect_b32 s15, s15, 16
	s_cmp_eq_u32 s15, s13
	s_cbranch_scc1 .LBB0_143
	s_mul_i32 s25, s15, 0x6000
	s_mul_hi_i32 s13, s15, 0x6000
	s_add_u32 s26, s60, s25
	s_addc_u32 s27, s63, s13
	v_lshl_add_u64 v[0:1], s[26:27], 0, v[70:71]
	s_mov_b64 s[26:27], 0x5000
	v_lshl_add_u64 v[16:17], v[0:1], 0, s[26:27]
	v_add_co_u32_e32 v0, vcc, 0x5000, v0
	s_mov_b32 s26, 0x3d800000
	s_nop 0
	v_addc_co_u32_e32 v1, vcc, 0, v1, vcc
	global_load_dwordx4 v[0:3], v[0:1], off
	s_nop 0
	global_load_dwordx4 v[4:7], v[16:17], off offset:16
	global_load_dwordx4 v[20:23], v[16:17], off offset:2064
	s_nop 0
	global_load_dwordx4 v[16:19], v[16:17], off offset:2048
	s_add_i32 s13, s15, 17
	s_add_i32 s25, s25, 0x66000
	s_mul_hi_i32 s13, s13, 0x6000
	global_load_dwordx4 v[40:43], v[64:65], off offset:16
	global_load_dwordx4 v[44:47], v[64:65], off
	s_waitcnt vmcnt(5)
	v_pk_mul_f32 v[2:3], v[2:3], s[26:27] op_sel_hi:[1,0]
	v_pk_mul_f32 v[0:1], v[0:1], s[26:27] op_sel_hi:[1,0]
	s_waitcnt vmcnt(4)
	v_pk_mul_f32 v[6:7], v[6:7], s[26:27] op_sel_hi:[1,0]
	v_pk_mul_f32 v[4:5], v[4:5], s[26:27] op_sel_hi:[1,0]
	s_waitcnt vmcnt(2)
	v_pk_mul_f32 v[18:19], v[18:19], s[26:27] op_sel_hi:[1,0]
	v_pk_mul_f32 v[16:17], v[16:17], s[26:27] op_sel_hi:[1,0]
	v_pk_mul_f32 v[22:23], v[22:23], s[26:27] op_sel_hi:[1,0]
	v_pk_mul_f32 v[20:21], v[20:21], s[26:27] op_sel_hi:[1,0]
	s_add_u32 s26, s60, s25
	s_addc_u32 s27, s63, s13
	v_lshl_add_u64 v[128:129], s[26:27], 0, v[70:71]
	s_movk_i32 s13, 0x1000
	v_add_co_u32_e32 v24, vcc, s13, v128
	v_lshl_add_u64 v[88:89], v[128:129], 0, s[84:85]
	s_nop 0
	v_addc_co_u32_e32 v25, vcc, 0, v129, vcc
	global_load_dwordx4 v[74:77], v[24:25], off
	global_load_dwordx4 v[78:81], v[88:89], off offset:16
	s_nop 0
	global_load_dwordx4 v[24:27], v[128:129], off offset:16
	global_load_dwordx4 v[28:31], v[128:129], off
	global_load_dwordx4 v[120:123], v[64:65], off offset:2048
	global_load_dwordx4 v[124:127], v[64:65], off offset:2064
	global_load_dwordx4 v[82:85], v[88:89], off offset:2064
	s_nop 0
	global_load_dwordx4 v[88:91], v[88:89], off offset:2048
	s_mov_b32 s13, s15
	s_waitcnt vmcnt(7)
	v_pk_add_f32 v[76:77], v[76:77], 1.0 op_sel_hi:[1,0]
	v_pk_add_f32 v[74:75], v[74:75], 1.0 op_sel_hi:[1,0]
	s_waitcnt vmcnt(6)
	v_pk_add_f32 v[80:81], v[80:81], 1.0 op_sel_hi:[1,0]
	v_pk_add_f32 v[130:131], v[78:79], 1.0 op_sel_hi:[1,0]
	v_pk_mul_f32 v[76:77], v[46:47], v[76:77]
	v_pk_mul_f32 v[78:79], v[42:43], v[80:81]
	v_pk_mul_f32 v[74:75], v[44:45], v[74:75]
	v_pk_mul_f32 v[80:81], v[40:41], v[130:131]
	global_load_dwordx4 v[40:43], v[128:129], off offset:2064
	global_load_dwordx4 v[44:47], v[128:129], off offset:2048
	s_waitcnt vmcnt(2)
	v_pk_add_f32 v[90:91], v[90:91], 1.0 op_sel_hi:[1,0]
	v_pk_add_f32 v[84:85], v[84:85], 1.0 op_sel_hi:[1,0]
	v_pk_add_f32 v[132:133], v[88:89], 1.0 op_sel_hi:[1,0]
	v_pk_add_f32 v[134:135], v[82:83], 1.0 op_sel_hi:[1,0]
	v_pk_mul_f32 v[88:89], v[126:127], v[84:85]
	v_pk_mul_f32 v[82:83], v[122:123], v[90:91]
	v_pk_mul_f32 v[90:91], v[124:125], v[134:135]
	v_pk_mul_f32 v[84:85], v[120:121], v[132:133]

.LBB0_1223:
	s_waitcnt vmcnt(0)
	v_cvt_pk_f32_fp8_sdwa v[40:41], v60 src0_sel:WORD_1
	v_cvt_pk_f32_fp8_e32 v[42:43], v60
	v_cvt_pk_f32_fp8_sdwa v[44:45], v61 src0_sel:WORD_1
	v_cvt_pk_f32_fp8_e32 v[46:47], v61
	v_cvt_pk_f32_fp8_e32 v[88:89], v58
	v_cvt_pk_f32_fp8_sdwa v[90:91], v58 src0_sel:WORD_1
	v_cvt_pk_f32_fp8_e32 v[92:93], v59
	v_cvt_pk_f32_fp8_sdwa v[94:95], v59 src0_sel:WORD_1
	v_pk_add_f32 v[40:41], v[40:41], 0 op_sel_hi:[1,0]
	v_pk_add_f32 v[42:43], v[42:43], 0 op_sel_hi:[1,0]
	v_pk_add_f32 v[44:45], v[44:45], 0 op_sel_hi:[1,0]
	v_pk_add_f32 v[46:47], v[46:47], 0 op_sel_hi:[1,0]
	v_pk_add_f32 v[42:43], v[42:43], v[88:89]
	v_pk_add_f32 v[40:41], v[40:41], v[90:91]
	v_pk_add_f32 v[46:47], v[46:47], v[92:93]
	v_pk_add_f32 v[44:45], v[44:45], v[94:95]
	v_cvt_pk_f32_fp8_sdwa v[88:89], v70 src0_sel:WORD_1
	v_cvt_pk_f32_fp8_e32 v[90:91], v70
	v_cvt_pk_f32_fp8_sdwa v[92:93], v71 src0_sel:WORD_1
	v_cvt_pk_f32_fp8_e32 v[94:95], v71
	s_add_i32 s10, s18, 1
	s_ashr_i32 s9, s8, 31
	s_ashr_i32 s11, s10, 31
	s_lshl_b64 s[12:13], s[8:9], 24
	s_lshl_b64 s[10:11], s[10:11], 12
	v_pk_add_f32 v[40:41], v[40:41], v[88:89]
	v_pk_add_f32 v[42:43], v[42:43], v[90:91]
	v_pk_add_f32 v[44:45], v[44:45], v[92:93]
	v_pk_add_f32 v[46:47], v[46:47], v[94:95]
	v_cvt_pk_f32_fp8_e32 v[88:89], v68
	v_cvt_pk_f32_fp8_sdwa v[90:91], v68 src0_sel:WORD_1
	v_cvt_pk_f32_fp8_e32 v[92:93], v69
	v_cvt_pk_f32_fp8_sdwa v[94:95], v69 src0_sel:WORD_1
	s_add_u32 s2, s92, s12
	s_addc_u32 s9, s93, s13
	s_add_u32 s10, s2, s10
	v_pk_add_f32 v[88:89], v[42:43], v[88:89]
	v_pk_add_f32 v[40:41], v[40:41], v[90:91]
	v_pk_add_f32 v[90:91], v[46:47], v[92:93]
	v_pk_add_f32 v[44:45], v[44:45], v[94:95]
	v_lshlrev_b32_e32 v46, 16, v4
	v_and_b32_e32 v47, 0xffff0000, v4
	v_lshlrev_b32_e32 v42, 16, v5
	v_and_b32_e32 v43, 0xffff0000, v5
	v_lshlrev_b32_e32 v94, 16, v7
	v_and_b32_e32 v95, 0xffff0000, v7
	s_addc_u32 s11, s9, s11
	v_lshlrev_b32_e32 v92, 16, v6
	v_and_b32_e32 v93, 0xffff0000, v6
	v_pk_fma_f32 v[42:43], v[34:35], v[40:41], v[42:43]
	v_pk_fma_f32 v[40:41], v[32:33], v[88:89], v[46:47]
	v_pk_fma_f32 v[46:47], v[26:27], v[44:45], v[94:95]
	v_lshl_add_u64 v[88:89], v[50:51], 2, s[10:11]
	v_pk_fma_f32 v[44:45], v[24:25], v[90:91], v[92:93]
	global_store_dwordx4 v[88:89], v[40:43], off nt
	global_store_dwordx4 v[88:89], v[44:47], off offset:16 nt
	v_cvt_pk_f32_fp8_e32 v[90:91], v56
	v_cvt_pk_f32_fp8_sdwa v[40:41], v62 src0_sel:WORD_1
	v_cvt_pk_f32_fp8_e32 v[42:43], v62
	v_cvt_pk_f32_fp8_e32 v[46:47], v63
	v_cvt_pk_f32_fp8_sdwa v[44:45], v63 src0_sel:WORD_1
	v_cvt_pk_f32_fp8_sdwa v[92:93], v56 src0_sel:WORD_1
	v_cvt_pk_f32_fp8_e32 v[94:95], v57
	v_cvt_pk_f32_fp8_sdwa v[96:97], v57 src0_sel:WORD_1
	v_pk_add_f32 v[40:41], v[40:41], 0 op_sel_hi:[1,0]
	v_pk_add_f32 v[42:43], v[42:43], 0 op_sel_hi:[1,0]
	v_pk_add_f32 v[46:47], v[46:47], 0 op_sel_hi:[1,0]
	v_pk_add_f32 v[44:45], v[44:45], 0 op_sel_hi:[1,0]
	v_pk_add_f32 v[42:43], v[42:43], v[90:91]
	v_pk_add_f32 v[40:41], v[40:41], v[92:93]
	v_pk_add_f32 v[46:47], v[46:47], v[94:95]
	v_cvt_pk_f32_fp8_sdwa v[90:91], v66 src0_sel:WORD_1
	v_cvt_pk_f32_fp8_e32 v[92:93], v66
	v_cvt_pk_f32_fp8_sdwa v[94:95], v67 src0_sel:WORD_1
	v_pk_add_f32 v[44:45], v[44:45], v[96:97]
	v_cvt_pk_f32_fp8_e32 v[96:97], v67
	v_pk_add_f32 v[40:41], v[40:41], v[90:91]
	v_pk_add_f32 v[42:43], v[42:43], v[92:93]
	v_pk_add_f32 v[44:45], v[44:45], v[94:95]
	v_cvt_pk_f32_fp8_e32 v[90:91], v64
	v_cvt_pk_f32_fp8_sdwa v[92:93], v64 src0_sel:WORD_1
	v_cvt_pk_f32_fp8_e32 v[94:95], v65
	v_pk_add_f32 v[46:47], v[46:47], v[96:97]
	v_cvt_pk_f32_fp8_sdwa v[96:97], v65 src0_sel:WORD_1
	v_pk_add_f32 v[90:91], v[42:43], v[90:91]
	v_pk_add_f32 v[40:41], v[40:41], v[92:93]
	v_pk_add_f32 v[92:93], v[46:47], v[94:95]
	v_lshlrev_b32_e32 v46, 16, v0
	v_and_b32_e32 v47, 0xffff0000, v0
	v_lshlrev_b32_e32 v42, 16, v1
	v_and_b32_e32 v43, 0xffff0000, v1
	v_pk_add_f32 v[44:45], v[44:45], v[96:97]
	v_lshlrev_b32_e32 v94, 16, v2
	v_and_b32_e32 v95, 0xffff0000, v2
	v_lshlrev_b32_e32 v96, 16, v3
	v_and_b32_e32 v97, 0xffff0000, v3
	v_pk_fma_f32 v[42:43], v[30:31], v[40:41], v[42:43]
	v_pk_fma_f32 v[40:41], v[28:29], v[90:91], v[46:47]
	v_pk_fma_f32 v[46:47], v[38:39], v[44:45], v[96:97]
	v_pk_fma_f32 v[44:45], v[36:37], v[92:93], v[94:95]
	global_store_dwordx4 v[88:89], v[40:43], off offset:2048 nt
	global_store_dwordx4 v[88:89], v[44:47], off offset:2064 nt

.LBB0_1225:
	s_add_i32 s17, s16, 0x100
	s_add_i32 s2, s16, 0x102
	s_cmp_lt_i32 s17, s5
	s_cselect_b32 s10, s2, s17
	s_ashr_i32 s11, s10, 31
	s_lshl_b64 s[10:11], s[10:11], 4
	v_readlane_b32 s12, v252, 8
	v_readlane_b32 s13, v252, 9
	s_add_u32 s10, s12, s10
	s_addc_u32 s11, s13, s11
	global_load_dwordx4 v[16:19], v49, s[10:11] offset:16
	global_load_dwordx4 v[20:23], v49, s[10:11]
	s_mul_hi_i32 s2, s17, 0x78787879
	s_lshr_b32 s8, s2, 31
	s_ashr_i32 s2, s2, 11
	s_add_i32 s12, s2, s8
	s_mul_i32 s2, s12, 0xffffef00
	s_add_i32 s2, s16, s2
	s_add_i32 s8, s2, 0x100
	s_cmpk_gt_i32 s8, 0xff
	s_cselect_b64 s[14:15], -1, 0
	s_cmpk_lt_i32 s8, 0x100
	s_cbranch_scc1 .LBB0_1227
	s_waitcnt vmcnt(0)
	v_mov_b32_e32 v48, v44
	v_lshlrev_b64 v[72:73], 10, v[48:49]
	v_mov_b32_e32 v48, v45
	v_lshlrev_b64 v[44:45], 10, v[48:49]
	v_mov_b32_e32 v48, v46
	v_lshl_add_u64 v[88:89], v[52:53], 0, v[72:73]
	v_lshlrev_b64 v[72:73], 10, v[48:49]
	v_mov_b32_e32 v48, v47
	v_lshlrev_b64 v[46:47], 10, v[48:49]
	global_load_dwordx4 v[12:15], v[54:55], off
	global_load_dwordx4 v[8:11], v[54:55], off offset:1024
	v_lshl_add_u64 v[44:45], v[52:53], 0, v[44:45]
	v_lshl_add_u64 v[90:91], v[52:53], 0, v[72:73]
	v_lshl_add_u64 v[46:47], v[52:53], 0, v[46:47]
	global_load_dwordx2 v[76:77], v[88:89], off nt
	global_load_dwordx2 v[74:75], v[44:45], off nt
	global_load_dwordx2 v[72:73], v[44:45], off offset:512 nt
	global_load_dwordx2 v[78:79], v[88:89], off offset:512 nt
	global_load_dwordx2 v[86:87], v[90:91], off nt
	global_load_dwordx2 v[84:85], v[46:47], off nt
	global_load_dwordx2 v[80:81], v[46:47], off offset:512 nt
	global_load_dwordx2 v[82:83], v[90:91], off offset:512 nt

.LBB0_1232:
	s_waitcnt vmcnt(0)
	v_mov_b32_e32 v48, v40
	v_lshlrev_b64 v[44:45], 10, v[48:49]
	v_mov_b32_e32 v48, v41
	v_lshlrev_b64 v[40:41], 10, v[48:49]
	v_mov_b32_e32 v48, v42
	v_lshlrev_b64 v[46:47], 10, v[48:49]
	v_mov_b32_e32 v48, v43
	v_lshl_add_u64 v[44:45], v[52:53], 0, v[44:45]
	v_lshlrev_b64 v[42:43], 10, v[48:49]
	global_load_dwordx4 v[4:7], v[54:55], off offset:2048
	global_load_dwordx4 v[0:3], v[54:55], off offset:3072
	v_lshl_add_u64 v[40:41], v[52:53], 0, v[40:41]
	v_lshl_add_u64 v[46:47], v[52:53], 0, v[46:47]
	v_lshl_add_u64 v[42:43], v[52:53], 0, v[42:43]
	global_load_dwordx2 v[60:61], v[44:45], off nt
	global_load_dwordx2 v[58:59], v[40:41], off nt
	global_load_dwordx2 v[56:57], v[40:41], off offset:512 nt
	global_load_dwordx2 v[62:63], v[44:45], off offset:512 nt
	global_load_dwordx2 v[70:71], v[46:47], off nt
	global_load_dwordx2 v[68:69], v[42:43], off nt
	global_load_dwordx2 v[64:65], v[42:43], off offset:512 nt
	global_load_dwordx2 v[66:67], v[46:47], off offset:512 nt
	s_andn2_b64 vcc, exec, s[14:15]
	s_cbranch_vccnz .LBB0_1229

.LBB0_1235:
	s_waitcnt vmcnt(0)
	v_cvt_pk_f32_fp8_sdwa v[40:41], v76 src0_sel:WORD_1
	v_cvt_pk_f32_fp8_e32 v[42:43], v76
	v_cvt_pk_f32_fp8_sdwa v[44:45], v77 src0_sel:WORD_1
	v_cvt_pk_f32_fp8_e32 v[46:47], v77
	v_cvt_pk_f32_fp8_e32 v[88:89], v74
	v_cvt_pk_f32_fp8_sdwa v[90:91], v74 src0_sel:WORD_1
	v_cvt_pk_f32_fp8_e32 v[92:93], v75
	v_cvt_pk_f32_fp8_sdwa v[94:95], v75 src0_sel:WORD_1
	v_pk_add_f32 v[40:41], v[40:41], 0 op_sel_hi:[1,0]
	v_pk_add_f32 v[42:43], v[42:43], 0 op_sel_hi:[1,0]
	v_pk_add_f32 v[44:45], v[44:45], 0 op_sel_hi:[1,0]
	v_pk_add_f32 v[46:47], v[46:47], 0 op_sel_hi:[1,0]
	v_pk_add_f32 v[42:43], v[42:43], v[88:89]
	v_pk_add_f32 v[40:41], v[40:41], v[90:91]
	v_pk_add_f32 v[46:47], v[46:47], v[92:93]
	v_pk_add_f32 v[44:45], v[44:45], v[94:95]
	v_cvt_pk_f32_fp8_sdwa v[88:89], v86 src0_sel:WORD_1
	v_cvt_pk_f32_fp8_e32 v[90:91], v86
	v_cvt_pk_f32_fp8_sdwa v[92:93], v87 src0_sel:WORD_1
	v_cvt_pk_f32_fp8_e32 v[94:95], v87
	s_ashr_i32 s13, s12, 31
	s_lshl_b64 s[12:13], s[12:13], 24
	s_lshl_b64 s[14:15], s[2:3], 12
	v_pk_add_f32 v[40:41], v[40:41], v[88:89]
	v_pk_add_f32 v[42:43], v[42:43], v[90:91]
	v_pk_add_f32 v[44:45], v[44:45], v[92:93]
	v_pk_add_f32 v[46:47], v[46:47], v[94:95]
	v_cvt_pk_f32_fp8_e32 v[88:89], v84
	v_cvt_pk_f32_fp8_sdwa v[90:91], v84 src0_sel:WORD_1
	v_cvt_pk_f32_fp8_e32 v[92:93], v85
	v_cvt_pk_f32_fp8_sdwa v[94:95], v85 src0_sel:WORD_1
	s_add_u32 s2, s92, s12
	s_addc_u32 s13, s93, s13
	s_add_u32 s12, s2, s14
	v_pk_add_f32 v[88:89], v[42:43], v[88:89]
	v_pk_add_f32 v[40:41], v[40:41], v[90:91]
	v_pk_add_f32 v[90:91], v[46:47], v[92:93]
	v_pk_add_f32 v[44:45], v[44:45], v[94:95]
	v_lshlrev_b32_e32 v46, 16, v12
	v_and_b32_e32 v47, 0xffff0000, v12
	v_lshlrev_b32_e32 v42, 16, v13
	v_and_b32_e32 v43, 0xffff0000, v13
	v_lshlrev_b32_e32 v94, 16, v15
	v_and_b32_e32 v95, 0xffff0000, v15
	s_addc_u32 s13, s13, s15
	v_lshlrev_b32_e32 v92, 16, v14
	v_and_b32_e32 v93, 0xffff0000, v14
	v_pk_fma_f32 v[42:43], v[34:35], v[40:41], v[42:43]
	v_pk_fma_f32 v[40:41], v[32:33], v[88:89], v[46:47]
	v_pk_fma_f32 v[46:47], v[26:27], v[44:45], v[94:95]
	v_lshl_add_u64 v[88:89], v[50:51], 2, s[12:13]
	v_pk_fma_f32 v[44:45], v[24:25], v[90:91], v[92:93]
	global_store_dwordx4 v[88:89], v[40:43], off nt
	global_store_dwordx4 v[88:89], v[44:47], off offset:16 nt
	v_cvt_pk_f32_fp8_e32 v[90:91], v72
	v_cvt_pk_f32_fp8_sdwa v[40:41], v78 src0_sel:WORD_1
	v_cvt_pk_f32_fp8_e32 v[42:43], v78
	v_cvt_pk_f32_fp8_e32 v[46:47], v79
	v_cvt_pk_f32_fp8_sdwa v[44:45], v79 src0_sel:WORD_1
	v_cvt_pk_f32_fp8_sdwa v[92:93], v72 src0_sel:WORD_1
	v_cvt_pk_f32_fp8_e32 v[94:95], v73
	v_cvt_pk_f32_fp8_sdwa v[96:97], v73 src0_sel:WORD_1
	v_pk_add_f32 v[40:41], v[40:41], 0 op_sel_hi:[1,0]
	v_pk_add_f32 v[42:43], v[42:43], 0 op_sel_hi:[1,0]
	v_pk_add_f32 v[46:47], v[46:47], 0 op_sel_hi:[1,0]
	v_pk_add_f32 v[44:45], v[44:45], 0 op_sel_hi:[1,0]
	v_pk_add_f32 v[42:43], v[42:43], v[90:91]
	v_pk_add_f32 v[40:41], v[40:41], v[92:93]
	v_pk_add_f32 v[46:47], v[46:47], v[94:95]
	v_cvt_pk_f32_fp8_sdwa v[90:91], v82 src0_sel:WORD_1
	v_cvt_pk_f32_fp8_e32 v[92:93], v82
	v_cvt_pk_f32_fp8_sdwa v[94:95], v83 src0_sel:WORD_1
	v_pk_add_f32 v[44:45], v[44:45], v[96:97]
	v_cvt_pk_f32_fp8_e32 v[96:97], v83
	v_pk_add_f32 v[40:41], v[40:41], v[90:91]
	v_pk_add_f32 v[42:43], v[42:43], v[92:93]
	v_pk_add_f32 v[44:45], v[44:45], v[94:95]
	v_cvt_pk_f32_fp8_e32 v[90:91], v80
	v_cvt_pk_f32_fp8_sdwa v[92:93], v80 src0_sel:WORD_1
	v_cvt_pk_f32_fp8_e32 v[94:95], v81
	v_pk_add_f32 v[46:47], v[46:47], v[96:97]
	v_cvt_pk_f32_fp8_sdwa v[96:97], v81 src0_sel:WORD_1
	v_pk_add_f32 v[90:91], v[42:43], v[90:91]
	v_pk_add_f32 v[40:41], v[40:41], v[92:93]
	v_pk_add_f32 v[92:93], v[46:47], v[94:95]
	v_lshlrev_b32_e32 v46, 16, v8
	v_and_b32_e32 v47, 0xffff0000, v8
	v_lshlrev_b32_e32 v42, 16, v9
	v_and_b32_e32 v43, 0xffff0000, v9
	v_pk_add_f32 v[44:45], v[44:45], v[96:97]
	v_lshlrev_b32_e32 v94, 16, v10
	v_and_b32_e32 v95, 0xffff0000, v10
	v_lshlrev_b32_e32 v96, 16, v11
	v_and_b32_e32 v97, 0xffff0000, v11
	v_pk_fma_f32 v[42:43], v[30:31], v[40:41], v[42:43]
	v_pk_fma_f32 v[40:41], v[28:29], v[90:91], v[46:47]
	v_pk_fma_f32 v[46:47], v[38:39], v[44:45], v[96:97]
	v_pk_fma_f32 v[44:45], v[36:37], v[92:93], v[94:95]
	global_store_dwordx4 v[88:89], v[40:43], off offset:2048 nt
	global_store_dwordx4 v[88:89], v[44:47], off offset:2064 nt
	s_andn2_b64 vcc, exec, s[10:11]
	s_cbranch_vccz .LBB0_1230
